# baseline (speedup 1.0000x reference)
.LBB1_19:
	s_or_b64 exec, exec, s[0:1]
	v_lshlrev_b32_e32 v1, 2, v0
	s_waitcnt lgkmcnt(0)
	s_barrier
	ds_read2st64_b32 v[2:3], v1 offset1:4
	v_add_u32_e32 v0, s11, v0
	v_ashrrev_i32_e32 v1, 31, v0
	v_lshl_add_u64 v[4:5], v[0:1], 2, s[6:7]
	v_add_u32_e32 v0, 0x100, v0
	v_ashrrev_i32_e32 v1, 31, v0
	v_lshl_add_u64 v[0:1], v[0:1], 2, s[6:7]
	s_waitcnt lgkmcnt(0)
	global_store_dword v[4:5], v2, off nt
	global_store_dword v[0:1], v3, off nt
	s_endpgm
